# P10 final LayerNorm loop: next-token register copies moved behind one end-of-iteration vmcnt so the prefetched rows get the whole iteration to land
# speedup vs baseline: 1.0069x; 1.0069x over previous
.LBB0_1362:
	v_cvt_pk_f32_fp8_sdwa v[182:183], v128 src0_sel:WORD_1
	v_cvt_pk_f32_fp8_e32 v[184:185], v128
	v_cvt_pk_f32_fp8_sdwa v[186:187], v129 src0_sel:WORD_1
	v_cvt_pk_f32_fp8_e32 v[194:195], v124
	v_cvt_pk_f32_fp8_sdwa v[196:197], v124 src0_sel:WORD_1
	v_cvt_pk_f32_fp8_e32 v[198:199], v125
	v_cvt_pk_f32_fp8_sdwa v[124:125], v125 src0_sel:WORD_1
	v_pk_add_f32 v[182:183], v[182:183], 0 op_sel_hi:[1,0]
	v_pk_add_f32 v[184:185], v[184:185], 0 op_sel_hi:[1,0]
	v_pk_add_f32 v[186:187], v[186:187], 0 op_sel_hi:[1,0]
	v_cvt_pk_f32_fp8_sdwa v[188:189], v130 src0_sel:WORD_1
	v_cvt_pk_f32_fp8_e32 v[190:191], v130
	v_cvt_pk_f32_fp8_sdwa v[192:193], v131 src0_sel:WORD_1
	v_pk_add_f32 v[184:185], v[184:185], v[194:195]
	v_pk_add_f32 v[182:183], v[182:183], v[196:197]
	v_pk_add_f32 v[124:125], v[186:187], v[124:125]
	v_cvt_pk_f32_fp8_e32 v[186:187], v126
	v_cvt_pk_f32_fp8_sdwa v[194:195], v126 src0_sel:WORD_1
	v_cvt_pk_f32_fp8_e32 v[196:197], v127
	v_cvt_pk_f32_fp8_sdwa v[126:127], v127 src0_sel:WORD_1
	v_cvt_pk_f32_fp8_e32 v[128:129], v129
	v_pk_add_f32 v[188:189], v[188:189], 0 op_sel_hi:[1,0]
	v_pk_add_f32 v[190:191], v[190:191], 0 op_sel_hi:[1,0]
	v_pk_add_f32 v[192:193], v[192:193], 0 op_sel_hi:[1,0]
	v_pk_add_f32 v[186:187], v[190:191], v[186:187]
	v_pk_add_f32 v[188:189], v[188:189], v[194:195]
	v_pk_add_f32 v[126:127], v[192:193], v[126:127]
	v_cvt_pk_f32_fp8_sdwa v[190:191], v120 src0_sel:WORD_1
	v_cvt_pk_f32_fp8_e32 v[192:193], v120
	v_cvt_pk_f32_fp8_sdwa v[194:195], v121 src0_sel:WORD_1
	v_cvt_pk_f32_fp8_e32 v[120:121], v121
	v_pk_add_f32 v[128:129], v[128:129], 0 op_sel_hi:[1,0]
	v_cvt_pk_f32_fp8_e32 v[130:131], v131
	v_pk_add_f32 v[128:129], v[128:129], v[198:199]
	v_pk_add_f32 v[182:183], v[182:183], v[190:191]
	v_pk_add_f32 v[184:185], v[184:185], v[192:193]
	v_pk_add_f32 v[120:121], v[128:129], v[120:121]
	v_cvt_pk_f32_fp8_sdwa v[128:129], v122 src0_sel:WORD_1
	v_cvt_pk_f32_fp8_e32 v[190:191], v122
	v_cvt_pk_f32_fp8_sdwa v[192:193], v123 src0_sel:WORD_1
	v_cvt_pk_f32_fp8_e32 v[122:123], v123
	v_pk_add_f32 v[130:131], v[130:131], 0 op_sel_hi:[1,0]
	v_pk_add_f32 v[128:129], v[188:189], v[128:129]
	v_pk_add_f32 v[130:131], v[130:131], v[196:197]
	v_pk_add_f32 v[186:187], v[186:187], v[190:191]
	v_pk_add_f32 v[122:123], v[130:131], v[122:123]
	v_cvt_pk_f32_fp8_e32 v[130:131], v116
	v_cvt_pk_f32_fp8_sdwa v[188:189], v116 src0_sel:WORD_1
	v_cvt_pk_f32_fp8_e32 v[190:191], v117
	v_cvt_pk_f32_fp8_sdwa v[116:117], v117 src0_sel:WORD_1
	v_pk_add_f32 v[124:125], v[124:125], v[194:195]
	v_pk_add_f32 v[130:131], v[184:185], v[130:131]
	v_pk_add_f32 v[182:183], v[182:183], v[188:189]
	v_pk_add_f32 v[184:185], v[120:121], v[190:191]
	v_pk_add_f32 v[116:117], v[124:125], v[116:117]
	v_cvt_pk_f32_fp8_e32 v[120:121], v118
	v_cvt_pk_f32_fp8_sdwa v[124:125], v118 src0_sel:WORD_1
	v_cvt_pk_f32_fp8_e32 v[188:189], v119
	v_cvt_pk_f32_fp8_sdwa v[118:119], v119 src0_sel:WORD_1
	v_mul_f32_e32 v174, 0x3f9837f0, v177
	v_pk_add_f32 v[126:127], v[126:127], v[192:193]
	v_mul_f32_e64 v176, v174, -v176
	v_pk_add_f32 v[126:127], v[126:127], v[118:119]
	v_lshlrev_b32_e32 v118, 16, v112
	v_and_b32_e32 v119, 0xffff0000, v112
	v_lshlrev_b32_e32 v112, 16, v113
	v_and_b32_e32 v113, 0xffff0000, v113
	v_pk_add_f32 v[124:125], v[128:129], v[124:125]
	v_pk_add_f32 v[128:129], v[122:123], v[188:189]
	v_lshlrev_b32_e32 v192, 16, v110
	v_and_b32_e32 v193, 0xffff0000, v110
	v_lshlrev_b32_e32 v194, 16, v111
	v_and_b32_e32 v195, 0xffff0000, v111
	v_pk_fma_f32 v[110:111], v[174:175], v[118:119], v[176:177] op_sel_hi:[0,1,0]
	v_pk_fma_f32 v[112:113], v[174:175], v[112:113], v[176:177] op_sel_hi:[0,1,0]
	s_waitcnt lgkmcnt(11)
	v_pk_fma_f32 v[118:119], v[182:183], s[8:9], v[162:163] op_sel_hi:[1,0,1]
	v_pk_fma_f32 v[122:123], v[130:131], s[8:9], v[160:161] op_sel_hi:[1,0,1]
	v_pk_add_f32 v[186:187], v[186:187], v[120:121]
	v_pk_fma_f32 v[120:121], v[112:113], v[158:159], v[118:119]
	v_pk_fma_f32 v[122:123], v[110:111], v[156:157], v[122:123]
	v_add_f32_e32 v111, v120, v121
	v_add_f32_e32 v110, v122, v123
	v_lshlrev_b32_e32 v188, 16, v114
	v_and_b32_e32 v189, 0xffff0000, v114
	v_lshlrev_b32_e32 v114, 16, v115
	v_and_b32_e32 v115, 0xffff0000, v115
	v_add_f32_e32 v110, v110, v111
	v_add_f32_e32 v118, 0, v110
	v_pk_fma_f32 v[112:113], v[174:175], v[188:189], v[176:177] op_sel_hi:[0,1,0]
	v_pk_fma_f32 v[110:111], v[174:175], v[114:115], v[176:177] op_sel_hi:[0,1,0]
	s_waitcnt lgkmcnt(10)
	v_pk_fma_f32 v[114:115], v[116:117], s[8:9], v[154:155] op_sel_hi:[1,0,1]
	v_pk_fma_f32 v[116:117], v[184:185], s[8:9], v[152:153] op_sel_hi:[1,0,1]
	v_pk_fma_f32 v[110:111], v[110:111], v[150:151], v[114:115]
	v_pk_fma_f32 v[116:117], v[112:113], v[148:149], v[116:117]
	v_add_f32_e32 v113, v110, v111
	v_add_f32_e32 v112, v116, v117
	v_lshlrev_b32_e32 v190, 16, v108
	v_and_b32_e32 v191, 0xffff0000, v108
	v_lshlrev_b32_e32 v108, 16, v109
	v_and_b32_e32 v109, 0xffff0000, v109
	v_add_f32_e32 v112, v112, v113
	v_add_f32_e32 v130, v118, v112
	v_pk_fma_f32 v[114:115], v[174:175], v[190:191], v[176:177] op_sel_hi:[0,1,0]
	v_pk_fma_f32 v[108:109], v[174:175], v[108:109], v[176:177] op_sel_hi:[0,1,0]
	s_waitcnt lgkmcnt(9)
	v_pk_fma_f32 v[112:113], v[124:125], s[8:9], v[146:147] op_sel_hi:[1,0,1]
	v_pk_fma_f32 v[118:119], v[186:187], s[8:9], v[144:145] op_sel_hi:[1,0,1]
	v_pk_fma_f32 v[112:113], v[108:109], v[142:143], v[112:113]
	v_pk_fma_f32 v[118:119], v[114:115], v[140:141], v[118:119]
	v_add_f32_e32 v109, v112, v113
	v_add_f32_e32 v108, v118, v119
	v_add_f32_e32 v108, v108, v109
	v_add_f32_e32 v130, v130, v108
	v_pk_fma_f32 v[114:115], v[174:175], v[192:193], v[176:177] op_sel_hi:[0,1,0]
	v_pk_fma_f32 v[108:109], v[174:175], v[194:195], v[176:177] op_sel_hi:[0,1,0]
	s_waitcnt lgkmcnt(8)
	v_pk_fma_f32 v[124:125], v[126:127], s[8:9], v[138:139] op_sel_hi:[1,0,1]
	v_pk_fma_f32 v[126:127], v[128:129], s[8:9], v[136:137] op_sel_hi:[1,0,1]
	v_pk_fma_f32 v[108:109], v[108:109], v[134:135], v[124:125]
	v_pk_fma_f32 v[114:115], v[114:115], v[132:133], v[126:127]
	v_add_f32_e32 v125, v108, v109
	v_add_f32_e32 v124, v114, v115
	v_add_f32_e32 v124, v124, v125
	v_add_f32_e32 v142, v130, v124
	v_cvt_pk_f32_fp8_sdwa v[124:125], v72 src0_sel:WORD_1
	v_cvt_pk_f32_fp8_e32 v[126:127], v72
	v_cvt_pk_f32_fp8_sdwa v[128:129], v73 src0_sel:WORD_1
	v_cvt_pk_f32_fp8_e32 v[136:137], v68
	v_cvt_pk_f32_fp8_sdwa v[138:139], v68 src0_sel:WORD_1
	v_cvt_pk_f32_fp8_e32 v[140:141], v69
	v_cvt_pk_f32_fp8_sdwa v[68:69], v69 src0_sel:WORD_1
	v_pk_add_f32 v[124:125], v[124:125], 0 op_sel_hi:[1,0]
	v_pk_add_f32 v[126:127], v[126:127], 0 op_sel_hi:[1,0]
	v_pk_add_f32 v[128:129], v[128:129], 0 op_sel_hi:[1,0]
	v_cvt_pk_f32_fp8_sdwa v[130:131], v74 src0_sel:WORD_1
	v_cvt_pk_f32_fp8_e32 v[132:133], v74
	v_cvt_pk_f32_fp8_sdwa v[134:135], v75 src0_sel:WORD_1
	v_pk_add_f32 v[126:127], v[126:127], v[136:137]
	v_pk_add_f32 v[124:125], v[124:125], v[138:139]
	v_pk_add_f32 v[68:69], v[128:129], v[68:69]
	v_cvt_pk_f32_fp8_e32 v[128:129], v70
	v_cvt_pk_f32_fp8_sdwa v[136:137], v70 src0_sel:WORD_1
	v_cvt_pk_f32_fp8_e32 v[138:139], v71
	v_cvt_pk_f32_fp8_sdwa v[70:71], v71 src0_sel:WORD_1
	v_cvt_pk_f32_fp8_e32 v[72:73], v73
	v_pk_add_f32 v[130:131], v[130:131], 0 op_sel_hi:[1,0]
	v_pk_add_f32 v[132:133], v[132:133], 0 op_sel_hi:[1,0]
	v_pk_add_f32 v[134:135], v[134:135], 0 op_sel_hi:[1,0]
	v_pk_add_f32 v[128:129], v[132:133], v[128:129]
	v_pk_add_f32 v[130:131], v[130:131], v[136:137]
	v_pk_add_f32 v[70:71], v[134:135], v[70:71]
	v_cvt_pk_f32_fp8_sdwa v[132:133], v64 src0_sel:WORD_1
	v_cvt_pk_f32_fp8_e32 v[134:135], v64
	v_cvt_pk_f32_fp8_sdwa v[136:137], v65 src0_sel:WORD_1
	v_cvt_pk_f32_fp8_e32 v[64:65], v65
	v_pk_add_f32 v[72:73], v[72:73], 0 op_sel_hi:[1,0]
	v_cvt_pk_f32_fp8_e32 v[74:75], v75
	v_pk_add_f32 v[72:73], v[72:73], v[140:141]
	v_pk_add_f32 v[124:125], v[124:125], v[132:133]
	v_pk_add_f32 v[126:127], v[126:127], v[134:135]
	v_pk_add_f32 v[64:65], v[72:73], v[64:65]
	v_cvt_pk_f32_fp8_sdwa v[72:73], v66 src0_sel:WORD_1
	v_cvt_pk_f32_fp8_e32 v[132:133], v66
	v_cvt_pk_f32_fp8_sdwa v[134:135], v67 src0_sel:WORD_1
	v_cvt_pk_f32_fp8_e32 v[66:67], v67
	v_pk_add_f32 v[74:75], v[74:75], 0 op_sel_hi:[1,0]
	v_pk_add_f32 v[72:73], v[130:131], v[72:73]
	v_pk_add_f32 v[74:75], v[74:75], v[138:139]
	v_pk_add_f32 v[128:129], v[128:129], v[132:133]
	v_pk_add_f32 v[66:67], v[74:75], v[66:67]
	v_cvt_pk_f32_fp8_e32 v[74:75], v60
	v_cvt_pk_f32_fp8_sdwa v[130:131], v60 src0_sel:WORD_1
	v_cvt_pk_f32_fp8_e32 v[132:133], v61
	v_cvt_pk_f32_fp8_sdwa v[60:61], v61 src0_sel:WORD_1
	v_pk_add_f32 v[68:69], v[68:69], v[136:137]
	v_pk_add_f32 v[74:75], v[126:127], v[74:75]
	v_pk_add_f32 v[124:125], v[124:125], v[130:131]
	v_pk_add_f32 v[60:61], v[68:69], v[60:61]
	v_cvt_pk_f32_fp8_e32 v[68:69], v62
	v_cvt_pk_f32_fp8_sdwa v[126:127], v62 src0_sel:WORD_1
	v_cvt_pk_f32_fp8_e32 v[130:131], v63
	v_cvt_pk_f32_fp8_sdwa v[62:63], v63 src0_sel:WORD_1
	v_pk_add_f32 v[70:71], v[70:71], v[134:135]
	v_pk_add_f32 v[72:73], v[72:73], v[126:127]
	v_pk_add_f32 v[126:127], v[66:67], v[130:131]
	v_pk_add_f32 v[70:71], v[70:71], v[62:63]
	v_lshlrev_b32_e32 v62, 16, v56
	v_and_b32_e32 v63, 0xffff0000, v56
	v_lshlrev_b32_e32 v56, 16, v57
	v_and_b32_e32 v57, 0xffff0000, v57
	v_pk_fma_f32 v[66:67], v[174:175], v[62:63], v[176:177] op_sel_hi:[0,1,0]
	v_pk_fma_f32 v[56:57], v[174:175], v[56:57], v[176:177] op_sel_hi:[0,1,0]
	s_waitcnt lgkmcnt(5)
	v_pk_fma_f32 v[62:63], v[124:125], s[8:9], v[106:107] op_sel_hi:[1,0,1]
	v_pk_fma_f32 v[74:75], v[74:75], s[8:9], v[104:105] op_sel_hi:[1,0,1]
	v_pk_fma_f32 v[62:63], v[56:57], v[102:103], v[62:63]
	v_pk_fma_f32 v[66:67], v[66:67], v[100:101], v[74:75]
	v_add_f32_e32 v57, v62, v63
	v_add_f32_e32 v56, v66, v67
	v_pk_add_f32 v[64:65], v[64:65], v[132:133]
	v_pk_add_f32 v[68:69], v[128:129], v[68:69]
	v_lshlrev_b32_e32 v128, 16, v58
	v_and_b32_e32 v129, 0xffff0000, v58
	v_lshlrev_b32_e32 v58, 16, v59
	v_and_b32_e32 v59, 0xffff0000, v59
	v_add_f32_e32 v56, v56, v57
	v_add_f32_e32 v100, v142, v56
	v_pk_fma_f32 v[74:75], v[174:175], v[128:129], v[176:177] op_sel_hi:[0,1,0]
	v_pk_fma_f32 v[56:57], v[174:175], v[58:59], v[176:177] op_sel_hi:[0,1,0]
	s_waitcnt lgkmcnt(4)
	v_pk_fma_f32 v[58:59], v[60:61], s[8:9], v[98:99] op_sel_hi:[1,0,1]
	v_pk_fma_f32 v[60:61], v[64:65], s[8:9], v[96:97] op_sel_hi:[1,0,1]
	v_pk_fma_f32 v[56:57], v[56:57], v[94:95], v[58:59]
	v_pk_fma_f32 v[64:65], v[74:75], v[92:93], v[60:61]
	v_add_f32_e32 v59, v56, v57
	v_add_f32_e32 v58, v64, v65
	v_lshlrev_b32_e32 v130, 16, v52
	v_and_b32_e32 v131, 0xffff0000, v52
	v_lshlrev_b32_e32 v52, 16, v53
	v_and_b32_e32 v53, 0xffff0000, v53
	v_add_f32_e32 v58, v58, v59
	v_add_f32_e32 v74, v100, v58
	v_pk_fma_f32 v[58:59], v[174:175], v[130:131], v[176:177] op_sel_hi:[0,1,0]
	v_pk_fma_f32 v[52:53], v[174:175], v[52:53], v[176:177] op_sel_hi:[0,1,0]
	s_waitcnt lgkmcnt(1)
	v_pk_fma_f32 v[60:61], v[72:73], s[8:9], v[90:91] op_sel_hi:[1,0,1]
	v_pk_fma_f32 v[68:69], v[68:69], s[8:9], v[88:89] op_sel_hi:[1,0,1]
	v_pk_fma_f32 v[60:61], v[52:53], v[86:87], v[60:61]
	v_pk_fma_f32 v[58:59], v[58:59], v[84:85], v[68:69]
	v_add_f32_e32 v53, v60, v61
	v_add_f32_e32 v52, v58, v59
	v_lshlrev_b32_e32 v132, 16, v54
	v_and_b32_e32 v133, 0xffff0000, v54
	v_lshlrev_b32_e32 v54, 16, v55
	v_and_b32_e32 v55, 0xffff0000, v55
	v_add_f32_e32 v52, v52, v53
	v_add_f32_e32 v72, v74, v52
	v_pk_fma_f32 v[52:53], v[174:175], v[132:133], v[176:177] op_sel_hi:[0,1,0]
	v_pk_fma_f32 v[54:55], v[174:175], v[54:55], v[176:177] op_sel_hi:[0,1,0]
	s_waitcnt lgkmcnt(0)
	v_pk_fma_f32 v[68:69], v[70:71], s[8:9], v[82:83] op_sel_hi:[1,0,1]
	v_pk_fma_f32 v[70:71], v[126:127], s[8:9], v[80:81] op_sel_hi:[1,0,1]
	v_pk_fma_f32 v[54:55], v[54:55], v[78:79], v[68:69]
	v_pk_fma_f32 v[52:53], v[52:53], v[76:77], v[70:71]
	v_add_f32_e32 v69, v54, v55
	v_add_f32_e32 v68, v52, v53
	v_add_f32_e32 v68, v68, v69
	v_and_b32_e32 v69, 64, v179
	v_add_u32_e32 v69, 64, v69
	v_xor_b32_e32 v70, 1, v179
	v_cmp_lt_i32_e32 vcc, v70, v69
	v_add_f32_e32 v68, v72, v68
	v_cndmask_b32_e32 v70, v179, v70, vcc
	v_lshlrev_b32_e32 v76, 2, v70
	ds_bpermute_b32 v70, v76, v68
	s_add_i32 s6, s6, s17
	s_waitcnt lgkmcnt(0)
	v_add_f32_e32 v68, v68, v70
	v_xor_b32_e32 v70, 2, v179
	v_cmp_lt_i32_e32 vcc, v70, v69
	s_nop 0
	v_cndmask_b32_e32 v70, v179, v70, vcc
	v_lshlrev_b32_e32 v77, 2, v70
	ds_bpermute_b32 v70, v77, v68
	s_waitcnt lgkmcnt(0)
	v_add_f32_e32 v68, v68, v70
	v_xor_b32_e32 v70, 4, v179
	v_cmp_lt_i32_e32 vcc, v70, v69
	s_nop 1
	v_cndmask_b32_e32 v70, v179, v70, vcc
	v_lshlrev_b32_e32 v78, 2, v70
	ds_bpermute_b32 v70, v78, v68
	s_waitcnt lgkmcnt(0)
	v_add_f32_e32 v68, v68, v70
	v_xor_b32_e32 v70, 8, v179
	v_cmp_lt_i32_e32 vcc, v70, v69
	s_nop 1
	v_cndmask_b32_e32 v70, v179, v70, vcc
	v_lshlrev_b32_e32 v79, 2, v70
	ds_bpermute_b32 v70, v79, v68
	s_waitcnt lgkmcnt(0)
	v_add_f32_e32 v68, v68, v70
	v_xor_b32_e32 v70, 16, v179
	v_cmp_lt_i32_e32 vcc, v70, v69
	s_nop 1
	v_cndmask_b32_e32 v70, v179, v70, vcc
	v_lshlrev_b32_e32 v80, 2, v70
	ds_bpermute_b32 v70, v80, v68
	s_waitcnt lgkmcnt(0)
	v_add_f32_e32 v68, v68, v70
	v_xor_b32_e32 v70, 32, v179
	v_cmp_lt_i32_e32 vcc, v70, v69
	s_nop 1
	v_cndmask_b32_e32 v69, v179, v70, vcc
	v_lshlrev_b32_e32 v81, 2, v69
	ds_bpermute_b32 v69, v81, v68
	s_waitcnt lgkmcnt(0)
	v_add_f32_e32 v82, v68, v69
	v_fmamk_f32 v123, v82, 0xba000000, v123
	v_fmamk_f32 v117, v82, 0xba000000, v117
	v_fmamk_f32 v121, v82, 0xba000000, v121
	v_fmac_f32_e32 v122, 0xba000000, v82
	v_fmamk_f32 v111, v82, 0xba000000, v111
	v_fmac_f32_e32 v116, 0xba000000, v82
	v_mov_b32_e32 v70, v123
	v_mov_b32_e32 v71, v117
	v_fmac_f32_e32 v120, 0xba000000, v82
	v_fmac_f32_e32 v110, 0xba000000, v82
	v_mov_b32_e32 v68, v122
	v_mov_b32_e32 v69, v116
	v_pk_mul_f32 v[70:71], v[70:71], v[70:71]
	v_mov_b32_e32 v72, v121
	v_mov_b32_e32 v73, v111
	v_pk_fma_f32 v[68:69], v[68:69], v[68:69], v[70:71]
	v_mov_b32_e32 v70, v120
	v_mov_b32_e32 v71, v110
	v_pk_mul_f32 v[72:73], v[72:73], v[72:73]
	v_fmamk_f32 v119, v82, 0xba000000, v119
	v_pk_fma_f32 v[70:71], v[70:71], v[70:71], v[72:73]
	v_fmac_f32_e32 v118, 0xba000000, v82
	v_pk_add_f32 v[68:69], v[68:69], v[70:71]
	v_fmamk_f32 v113, v82, 0xba000000, v113
	v_fmac_f32_e32 v112, 0xba000000, v82
	v_pk_add_f32 v[68:69], v[68:69], v[68:69] op_sel_hi:[0,1]
	v_pk_mul_f32 v[70:71], v[112:113], v[112:113]
	v_pk_mul_f32 v[72:73], v[118:119], v[118:119]
	v_fmac_f32_e32 v114, 0xba000000, v82
	v_pk_mov_b32 v[74:75], v[72:73], v[70:71] op_sel:[1,0]
	v_mov_b32_e32 v73, v71
	v_fmamk_f32 v115, v82, 0xba000000, v115
	v_fmac_f32_e32 v108, 0xba000000, v82
	v_mul_f32_e32 v68, v114, v114
	v_pk_add_f32 v[70:71], v[74:75], v[72:73]
	v_fmamk_f32 v109, v82, 0xba000000, v109
	v_pk_fma_f32 v[72:73], v[114:115], v[114:115], v[68:69] op_sel_hi:[1,1,0]
	v_mul_f32_e32 v68, v108, v108
	v_pk_add_f32 v[70:71], v[70:71], v[70:71] op_sel_hi:[0,1]
	v_pk_fma_f32 v[74:75], v[108:109], v[108:109], v[68:69] op_sel_hi:[1,1,0]
	v_fmamk_f32 v63, v82, 0xba000000, v63
	v_fmac_f32_e32 v62, 0xba000000, v82
	v_fmamk_f32 v67, v82, 0xba000000, v67
	v_fmac_f32_e32 v66, 0xba000000, v82
	v_mul_f32_e32 v72, v66, v66
	v_mul_f32_e32 v74, v67, v67
	v_mul_f32_e32 v70, v62, v62
	v_mul_f32_e32 v68, v63, v63
	v_pk_add_f32 v[72:73], v[72:73], v[74:75]
	v_pk_add_f32 v[68:69], v[70:71], v[68:69]
	v_fmamk_f32 v65, v82, 0xba000000, v65
	v_pk_add_f32 v[68:69], v[72:73], v[68:69]
	v_fmac_f32_e32 v64, 0xba000000, v82
	v_fmamk_f32 v57, v82, 0xba000000, v57
	v_fmac_f32_e32 v56, 0xba000000, v82
	v_pk_add_f32 v[68:69], v[68:69], v[68:69] op_sel_hi:[0,1]
	v_pk_mul_f32 v[70:71], v[56:57], v[56:57]
	v_pk_mul_f32 v[72:73], v[64:65], v[64:65]
	v_fmac_f32_e32 v58, 0xba000000, v82
	v_pk_mov_b32 v[74:75], v[72:73], v[70:71] op_sel:[1,0]
	v_mov_b32_e32 v73, v71
	v_fmamk_f32 v59, v82, 0xba000000, v59
	v_fmac_f32_e32 v60, 0xba000000, v82
	v_mul_f32_e32 v68, v58, v58
	v_pk_add_f32 v[70:71], v[74:75], v[72:73]
	v_fmamk_f32 v61, v82, 0xba000000, v61
	v_pk_fma_f32 v[72:73], v[58:59], v[58:59], v[68:69] op_sel_hi:[1,1,0]
	v_mul_f32_e32 v68, v60, v60
	v_pk_add_f32 v[70:71], v[70:71], v[70:71] op_sel_hi:[0,1]
	v_pk_fma_f32 v[74:75], v[60:61], v[60:61], v[68:69] op_sel_hi:[1,1,0]
	v_fmamk_f32 v55, v82, 0xba000000, v55
	v_fmac_f32_e32 v54, 0xba000000, v82
	v_fmamk_f32 v53, v82, 0xba000000, v53
	v_fmac_f32_e32 v52, 0xba000000, v82
	v_mul_f32_e32 v72, v52, v52
	v_mul_f32_e32 v74, v53, v53
	v_mul_f32_e32 v70, v54, v54
	v_mul_f32_e32 v68, v55, v55
	v_pk_add_f32 v[72:73], v[72:73], v[74:75]
	v_pk_add_f32 v[68:69], v[70:71], v[68:69]
	s_nop 0
	v_pk_add_f32 v[68:69], v[72:73], v[68:69]
	s_nop 0
	v_add_f32_e32 v68, v68, v69
	ds_bpermute_b32 v69, v76, v68
	s_waitcnt lgkmcnt(0)
	v_add_f32_e32 v68, v68, v69
	ds_bpermute_b32 v69, v77, v68
	s_waitcnt lgkmcnt(0)
	v_add_f32_e32 v68, v68, v69
	ds_bpermute_b32 v69, v78, v68
	s_waitcnt lgkmcnt(0)
	v_add_f32_e32 v68, v68, v69
	ds_bpermute_b32 v69, v79, v68
	s_waitcnt lgkmcnt(0)
	v_add_f32_e32 v68, v68, v69
	ds_bpermute_b32 v69, v80, v68
	s_waitcnt lgkmcnt(0)
	v_add_f32_e32 v68, v68, v69
	ds_bpermute_b32 v69, v81, v68
	s_waitcnt lgkmcnt(0)
	v_add_f32_e32 v68, v68, v69
	v_fmamk_f32 v68, v68, 0x3a000000, v165
	v_mul_f32_e32 v69, 0x4f800000, v68
	v_cmp_gt_f32_e32 vcc, s18, v68
	s_nop 1
	v_cndmask_b32_e32 v68, v68, v69, vcc
	v_sqrt_f32_e32 v69, v68
	s_nop 0
	v_add_u32_e32 v70, -1, v69
	v_fma_f32 v71, -v70, v69, v68
	v_cmp_ge_f32_e64 s[0:1], 0, v71
	v_add_u32_e32 v71, 1, v69
	s_nop 0
	v_cndmask_b32_e64 v70, v69, v70, s[0:1]
	v_fma_f32 v69, -v71, v69, v68
	v_cmp_lt_f32_e64 s[0:1], 0, v69
	s_nop 1
	v_cndmask_b32_e64 v69, v70, v71, s[0:1]
	v_mul_f32_e32 v70, 0x37800000, v69
	v_cndmask_b32_e32 v69, v69, v70, vcc
	v_cmp_class_f32_e32 vcc, v68, v178
	s_nop 1
	v_cndmask_b32_e32 v68, v69, v68, vcc
	v_div_scale_f32 v69, s[0:1], v68, v68, 1.0
	v_rcp_f32_e32 v70, v69
	s_mov_b32 s0, s10
	v_fma_f32 v71, -v69, v70, 1.0
	v_fmac_f32_e32 v70, v71, v70
	v_div_scale_f32 v71, vcc, 1.0, v68, 1.0
	v_mul_f32_e32 v72, v71, v70
	v_fma_f32 v73, -v69, v72, v71
	v_fmac_f32_e32 v72, v73, v70
	v_fma_f32 v69, -v69, v72, v71
	v_div_fmas_f32 v69, v69, v70, v72
	v_div_fixup_f32 v92, v69, v68, 1.0
	ds_read_b128 v[68:71], v180 offset:24576
	ds_read_b128 v[72:75], v180 offset:16384
	ds_read_b128 v[76:79], v180 offset:16400
	ds_read_b128 v[80:83], v180 offset:16416
	ds_read_b128 v[84:87], v180 offset:16432
	ds_read_b128 v[88:91], v180 offset:24592
	v_pk_mul_f32 v[94:95], v[122:123], v[92:93] op_sel_hi:[1,0]
	v_pk_mul_f32 v[96:97], v[120:121], v[92:93] op_sel_hi:[1,0]
	s_waitcnt lgkmcnt(4)
	v_pk_fma_f32 v[68:69], v[72:73], v[94:95], v[68:69]
	v_pk_fma_f32 v[70:71], v[74:75], v[96:97], v[70:71]
	global_store_dwordx4 v[170:171], v[68:71], off offset:-4096
	ds_read_b128 v[72:75], v180 offset:24608
	v_pk_mul_f32 v[62:63], v[62:63], v[92:93] op_sel_hi:[1,0]
	v_pk_mul_f32 v[68:69], v[116:117], v[92:93] op_sel_hi:[1,0]
	v_pk_mul_f32 v[70:71], v[110:111], v[92:93] op_sel_hi:[1,0]
	s_waitcnt lgkmcnt(1)
	v_pk_fma_f32 v[68:69], v[76:77], v[68:69], v[88:89]
	v_pk_fma_f32 v[70:71], v[78:79], v[70:71], v[90:91]
	global_store_dwordx4 v[170:171], v[68:71], off offset:-4080
	ds_read_b128 v[68:71], v180 offset:24624
	v_pk_mul_f32 v[76:77], v[118:119], v[92:93] op_sel_hi:[1,0]
	v_pk_mul_f32 v[78:79], v[112:113], v[92:93] op_sel_hi:[1,0]
	s_waitcnt lgkmcnt(1)
	v_pk_fma_f32 v[72:73], v[80:81], v[76:77], v[72:73]
	v_pk_fma_f32 v[74:75], v[82:83], v[78:79], v[74:75]
	global_store_dwordx4 v[170:171], v[72:75], off offset:-4064
	v_pk_mul_f32 v[66:67], v[66:67], v[92:93] op_sel_hi:[1,0]
	v_pk_mul_f32 v[56:57], v[56:57], v[92:93] op_sel_hi:[1,0]
	v_pk_mul_f32 v[72:73], v[114:115], v[92:93] op_sel_hi:[1,0]
	v_pk_mul_f32 v[74:75], v[108:109], v[92:93] op_sel_hi:[1,0]
	s_waitcnt lgkmcnt(0)
	v_pk_fma_f32 v[68:69], v[84:85], v[72:73], v[68:69]
	v_pk_fma_f32 v[70:71], v[86:87], v[74:75], v[70:71]
	global_store_dwordx4 v[170:171], v[68:71], off offset:-4048
	ds_read_b128 v[68:71], v180 offset:20480
	ds_read_b128 v[72:75], v180 offset:28672
	ds_read_b128 v[76:79], v180 offset:20496
	ds_read_b128 v[80:83], v180 offset:28688
	v_pk_mul_f32 v[54:55], v[54:55], v[92:93] op_sel_hi:[1,0]
	v_pk_mul_f32 v[52:53], v[52:53], v[92:93] op_sel_hi:[1,0]
	s_waitcnt lgkmcnt(2)
	v_pk_fma_f32 v[70:71], v[70:71], v[62:63], v[74:75]
	v_pk_mul_f32 v[62:63], v[64:65], v[92:93] op_sel_hi:[1,0]
	v_pk_fma_f32 v[68:69], v[68:69], v[66:67], v[72:73]
	s_waitcnt lgkmcnt(0)
	v_pk_fma_f32 v[64:65], v[78:79], v[56:57], v[82:83]
	v_pk_fma_f32 v[62:63], v[76:77], v[62:63], v[80:81]
	global_store_dwordx4 v[170:171], v[68:71], off
	global_store_dwordx4 v[170:171], v[62:65], off offset:16
	ds_read_b128 v[62:65], v180 offset:20512
	ds_read_b128 v[66:69], v180 offset:28704
	v_pk_mul_f32 v[74:75], v[60:61], v[92:93] op_sel_hi:[1,0]
	v_pk_mul_f32 v[60:61], v[58:59], v[92:93] op_sel_hi:[1,0]
	ds_read_b128 v[56:59], v180 offset:20528
	ds_read_b128 v[70:73], v180 offset:28720
	s_waitcnt lgkmcnt(2)
	v_pk_fma_f32 v[60:61], v[62:63], v[60:61], v[66:67]
	v_pk_fma_f32 v[62:63], v[64:65], v[74:75], v[68:69]
	global_store_dwordx4 v[170:171], v[60:63], off offset:32
	s_waitcnt lgkmcnt(0)
	v_pk_fma_f32 v[52:53], v[56:57], v[52:53], v[70:71]
	v_pk_fma_f32 v[54:55], v[58:59], v[54:55], v[72:73]
	global_store_dwordx4 v[170:171], v[52:55], off offset:48
	s_waitcnt vmcnt(8)
	v_mov_b64_e32 v[126:127], v[22:23]
	v_mov_b64_e32 v[130:131], v[38:39]
	v_mov_b64_e32 v[124:125], v[20:21]
	v_mov_b64_e32 v[128:129], v[36:37]
	v_mov_b64_e32 v[176:177], v[172:173]
	v_mov_b64_e32 v[118:119], v[30:31]
	v_mov_b64_e32 v[122:123], v[26:27]
	v_mov_b64_e32 v[62:63], v[14:15]
	v_mov_b64_e32 v[66:67], v[18:19]
	v_mov_b64_e32 v[70:71], v[10:11]
	v_mov_b64_e32 v[74:75], v[6:7]
	v_mov_b64_e32 v[54:55], v[42:43]
	v_mov_b64_e32 v[58:59], v[46:47]
	v_mov_b64_e32 v[110:111], v[50:51]
	v_mov_b64_e32 v[114:115], v[34:35]
	v_lshl_add_u64 v[170:171], v[170:171], 0, s[4:5]
	s_andn2_b64 vcc, exec, s[12:13]
	v_mov_b64_e32 v[60:61], v[12:13]
	v_mov_b64_e32 v[64:65], v[16:17]
	v_mov_b64_e32 v[68:69], v[8:9]
	v_mov_b64_e32 v[72:73], v[4:5]
	v_mov_b64_e32 v[116:117], v[28:29]
	v_mov_b64_e32 v[120:121], v[24:25]
	v_mov_b64_e32 v[52:53], v[40:41]
	v_mov_b64_e32 v[56:57], v[44:45]
	v_mov_b64_e32 v[108:109], v[48:49]
	v_mov_b64_e32 v[112:113], v[32:33]
	s_cbranch_vccz .LBB0_1366
